# MergeA epilogue: second row group's gate loads hoisted beside the first group's (into dead K-loop fragment registers)
# speedup vs baseline: 1.0056x; 1.0042x over previous
.LBB0_2143:
	s_add_u32 s22, s26, 0x100
	s_addc_u32 s23, s27, 0
	s_cmp_eq_u32 s58, 12
	s_cselect_b32 s29, s21, s23
	s_cselect_b32 s28, s20, s22
	s_cselect_b32 s25, s9, s57
	s_cselect_b32 s24, s8, s56
	s_add_i32 s59, 0, 0x10000
	v_add_u32_e32 v14, s59, v175
	ds_read_b128 v[2:5], v14
	ds_read_b128 v[6:9], v14 offset:1024
	ds_read_b128 v[10:13], v14 offset:2048
	ds_read_b128 v[14:17], v14 offset:3072
	v_lshl_add_u64 v[164:165], s[26:27], 0, v[162:163]
	s_add_i32 m0, s43, 0xc000
	ds_read_b128 v[178:181], v177
	ds_read_b128 v[182:185], v177 offset:1024
	ds_read_b128 v[186:189], v177 offset:2048
	ds_read_b128 v[190:193], v177 offset:3072
	ds_read_b128 v[194:197], v177 offset:4096
	ds_read_b128 v[198:201], v177 offset:5120
	ds_read_b128 v[202:205], v177 offset:6144
	ds_read_b128 v[206:209], v177 offset:7168
	global_load_lds_dwordx4 v[164:165], off
	v_lshl_add_u64 v[164:165], s[26:27], 0, v[160:161]
	s_add_i32 m0, s43, 0xe000
	s_nop 0
	global_load_lds_dwordx4 v[164:165], off
	s_waitcnt lgkmcnt(8)
	s_barrier
	s_waitcnt lgkmcnt(0)
	s_setprio 1
	s_waitcnt lgkmcnt(0)
	v_mfma_scale_f32_16x16x128_f8f6f4 v[142:145], v[2:9], v[178:185], v[142:145], v1, v1 op_sel_hi:[0,0,0]
	v_mfma_scale_f32_16x16x128_f8f6f4 v[138:141], v[10:17], v[178:185], v[138:141], v1, v1 op_sel_hi:[0,0,0]
	v_mfma_scale_f32_16x16x128_f8f6f4 v[126:129], v[2:9], v[186:193], v[126:129], v1, v1 op_sel_hi:[0,0,0]
	v_mfma_scale_f32_16x16x128_f8f6f4 v[122:125], v[10:17], v[186:193], v[122:125], v1, v1 op_sel_hi:[0,0,0]
	v_mfma_scale_f32_16x16x128_f8f6f4 v[110:113], v[2:9], v[194:201], v[110:113], v1, v1 op_sel_hi:[0,0,0]
	v_mfma_scale_f32_16x16x128_f8f6f4 v[106:109], v[10:17], v[194:201], v[106:109], v1, v1 op_sel_hi:[0,0,0]
	v_mfma_scale_f32_16x16x128_f8f6f4 v[94:97], v[2:9], v[202:209], v[94:97], v1, v1 op_sel_hi:[0,0,0]
	v_mfma_scale_f32_16x16x128_f8f6f4 v[90:93], v[10:17], v[202:209], v[90:93], v1, v1 op_sel_hi:[0,0,0]
	s_setprio 0
	s_barrier
	s_add_i32 s60, 0, 0x14000
	v_add_u32_e32 v164, s60, v175
	s_add_i32 s26, s59, s42
	ds_read_b128 v[210:213], v164
	ds_read_b128 v[214:217], v164 offset:1024
	ds_read_b128 v[218:221], v164 offset:2048
	ds_read_b128 v[222:225], v164 offset:3072
	v_lshl_add_u64 v[164:165], s[24:25], 0, v[146:147]
	s_mov_b32 m0, s26
	v_lshl_add_u64 v[166:167], s[24:25], 0, v[148:149]
	global_load_lds_dwordx4 v[164:165], off
	s_add_i32 m0, s26, 0x2000
	s_nop 0
	global_load_lds_dwordx4 v[166:167], off
	s_barrier
	s_waitcnt lgkmcnt(0)
	s_setprio 1
	s_waitcnt lgkmcnt(0)
	v_mfma_scale_f32_16x16x128_f8f6f4 v[134:137], v[210:217], v[178:185], v[134:137], v1, v1 op_sel_hi:[0,0,0]
	v_mfma_scale_f32_16x16x128_f8f6f4 v[130:133], v[218:225], v[178:185], v[130:133], v1, v1 op_sel_hi:[0,0,0]
	v_mfma_scale_f32_16x16x128_f8f6f4 v[118:121], v[210:217], v[186:193], v[118:121], v1, v1 op_sel_hi:[0,0,0]
	v_mfma_scale_f32_16x16x128_f8f6f4 v[114:117], v[218:225], v[186:193], v[114:117], v1, v1 op_sel_hi:[0,0,0]
	v_mfma_scale_f32_16x16x128_f8f6f4 v[102:105], v[210:217], v[194:201], v[102:105], v1, v1 op_sel_hi:[0,0,0]
	v_mfma_scale_f32_16x16x128_f8f6f4 v[98:101], v[218:225], v[194:201], v[98:101], v1, v1 op_sel_hi:[0,0,0]
	v_mfma_scale_f32_16x16x128_f8f6f4 v[86:89], v[210:217], v[202:209], v[86:89], v1, v1 op_sel_hi:[0,0,0]
	v_mfma_scale_f32_16x16x128_f8f6f4 v[82:85], v[218:225], v[202:209], v[82:85], v1, v1 op_sel_hi:[0,0,0]
	s_setprio 0
	s_mov_b32 m0, s43
	v_lshl_add_u64 v[168:169], s[28:29], 0, v[150:151]
	s_barrier
	ds_read_b128 v[178:181], v177 offset:16384
	ds_read_b128 v[182:185], v177 offset:17408
	ds_read_b128 v[186:189], v177 offset:18432
	ds_read_b128 v[190:193], v177 offset:19456
	ds_read_b128 v[194:197], v177 offset:20480
	ds_read_b128 v[198:201], v177 offset:21504
	ds_read_b128 v[202:205], v177 offset:22528
	ds_read_b128 v[206:209], v177 offset:23552
	global_load_lds_dwordx4 v[168:169], off
	v_lshl_add_u64 v[170:171], s[28:29], 0, v[152:153]
	s_mov_b32 m0, s44
	s_nop 0
	global_load_lds_dwordx4 v[170:171], off
	s_barrier
	s_waitcnt lgkmcnt(0)
	s_setprio 1
	s_waitcnt lgkmcnt(0)
	v_mfma_scale_f32_16x16x128_f8f6f4 v[78:81], v[2:9], v[178:185], v[78:81], v1, v1 op_sel_hi:[0,0,0]
	v_mfma_scale_f32_16x16x128_f8f6f4 v[74:77], v[10:17], v[178:185], v[74:77], v1, v1 op_sel_hi:[0,0,0]
	v_mfma_scale_f32_16x16x128_f8f6f4 v[62:65], v[2:9], v[186:193], v[62:65], v1, v1 op_sel_hi:[0,0,0]
	v_mfma_scale_f32_16x16x128_f8f6f4 v[58:61], v[10:17], v[186:193], v[58:61], v1, v1 op_sel_hi:[0,0,0]
	v_mfma_scale_f32_16x16x128_f8f6f4 v[42:45], v[2:9], v[194:201], v[42:45], v1, v1 op_sel_hi:[0,0,0]
	v_mfma_scale_f32_16x16x128_f8f6f4 v[34:37], v[10:17], v[194:201], v[34:37], v1, v1 op_sel_hi:[0,0,0]
	v_mfma_scale_f32_16x16x128_f8f6f4 v[22:25], v[2:9], v[202:209], v[22:25], v1, v1 op_sel_hi:[0,0,0]
	v_mfma_scale_f32_16x16x128_f8f6f4 v[18:21], v[10:17], v[202:209], v[18:21], v1, v1 op_sel_hi:[0,0,0]
	s_setprio 0
	s_barrier
	s_add_u32 s26, s24, 0x60000
	s_addc_u32 s27, s25, 0
	s_add_i32 s59, s60, s42
	v_lshl_add_u64 v[2:3], s[26:27], 0, v[146:147]
	s_mov_b32 m0, s59
	s_nop 0
	global_load_lds_dwordx4 v[2:3], off
	v_lshl_add_u64 v[2:3], s[26:27], 0, v[148:149]
	s_add_i32 m0, s59, 0x2000
	s_nop 0
	global_load_lds_dwordx4 v[2:3], off
	s_waitcnt vmcnt(6)
	s_barrier
	s_setprio 1
	v_mfma_scale_f32_16x16x128_f8f6f4 v[70:73], v[210:217], v[178:185], v[70:73], v1, v1 op_sel_hi:[0,0,0]
	v_mfma_scale_f32_16x16x128_f8f6f4 v[66:69], v[218:225], v[178:185], v[66:69], v1, v1 op_sel_hi:[0,0,0]
	v_mfma_scale_f32_16x16x128_f8f6f4 v[46:49], v[210:217], v[186:193], v[46:49], v1, v1 op_sel_hi:[0,0,0]
	v_mfma_scale_f32_16x16x128_f8f6f4 v[38:41], v[218:225], v[186:193], v[38:41], v1, v1 op_sel_hi:[0,0,0]
	v_mfma_scale_f32_16x16x128_f8f6f4 v[50:53], v[210:217], v[194:201], v[50:53], v1, v1 op_sel_hi:[0,0,0]
	v_mfma_scale_f32_16x16x128_f8f6f4 v[54:57], v[218:225], v[194:201], v[54:57], v1, v1 op_sel_hi:[0,0,0]
	v_mfma_scale_f32_16x16x128_f8f6f4 v[26:29], v[210:217], v[202:209], v[26:29], v1, v1 op_sel_hi:[0,0,0]
	v_mfma_scale_f32_16x16x128_f8f6f4 v[30:33], v[218:225], v[202:209], v[30:33], v1, v1 op_sel_hi:[0,0,0]
	s_setprio 0
	s_add_i32 s26, 0, 0x18000
	v_add_u32_e32 v14, s26, v175
	s_barrier
	ds_read_b128 v[2:5], v14
	ds_read_b128 v[6:9], v14 offset:1024
	ds_read_b128 v[10:13], v14 offset:2048
	ds_read_b128 v[14:17], v14 offset:3072
	s_mov_b32 m0, s45
	v_lshl_add_u64 v[210:211], s[28:29], 0, v[154:155]
	ds_read_b128 v[178:181], v177 offset:32768
	ds_read_b128 v[182:185], v177 offset:33792
	ds_read_b128 v[186:189], v177 offset:34816
	ds_read_b128 v[190:193], v177 offset:35840
	ds_read_b128 v[194:197], v177 offset:36864
	ds_read_b128 v[198:201], v177 offset:37888
	ds_read_b128 v[202:205], v177 offset:38912
	ds_read_b128 v[206:209], v177 offset:39936
	global_load_lds_dwordx4 v[210:211], off
	v_lshl_add_u64 v[210:211], s[28:29], 0, v[156:157]
	s_mov_b32 m0, s48
	s_nop 0
	global_load_lds_dwordx4 v[210:211], off
	s_waitcnt lgkmcnt(8)
	s_barrier
	s_waitcnt lgkmcnt(0)
	s_setprio 1
	s_waitcnt lgkmcnt(0)
	v_mfma_scale_f32_16x16x128_f8f6f4 v[142:145], v[2:9], v[178:185], v[142:145], v1, v1 op_sel_hi:[0,0,0]
	v_mfma_scale_f32_16x16x128_f8f6f4 v[138:141], v[10:17], v[178:185], v[138:141], v1, v1 op_sel_hi:[0,0,0]
	v_mfma_scale_f32_16x16x128_f8f6f4 v[126:129], v[2:9], v[186:193], v[126:129], v1, v1 op_sel_hi:[0,0,0]
	v_mfma_scale_f32_16x16x128_f8f6f4 v[122:125], v[10:17], v[186:193], v[122:125], v1, v1 op_sel_hi:[0,0,0]
	v_mfma_scale_f32_16x16x128_f8f6f4 v[110:113], v[2:9], v[194:201], v[110:113], v1, v1 op_sel_hi:[0,0,0]
	v_mfma_scale_f32_16x16x128_f8f6f4 v[106:109], v[10:17], v[194:201], v[106:109], v1, v1 op_sel_hi:[0,0,0]
	v_mfma_scale_f32_16x16x128_f8f6f4 v[94:97], v[2:9], v[202:209], v[94:97], v1, v1 op_sel_hi:[0,0,0]
	v_mfma_scale_f32_16x16x128_f8f6f4 v[90:93], v[10:17], v[202:209], v[90:93], v1, v1 op_sel_hi:[0,0,0]
	s_setprio 0
	s_barrier
	s_add_i32 s27, 0, 0x1c000
	s_add_i32 s26, s26, s42
	v_add_u32_e32 v222, s27, v175
	v_lshl_add_u64 v[164:165], v[164:165], 0, s[16:17]
	s_mov_b32 m0, s26
	ds_read_b128 v[210:213], v222
	ds_read_b128 v[214:217], v222 offset:1024
	ds_read_b128 v[218:221], v222 offset:2048
	ds_read_b128 v[222:225], v222 offset:3072
	global_load_lds_dwordx4 v[164:165], off
	v_lshl_add_u64 v[164:165], v[166:167], 0, s[16:17]
	s_add_i32 m0, s26, 0x2000
	s_nop 0
	global_load_lds_dwordx4 v[164:165], off
	s_barrier
	s_waitcnt lgkmcnt(0)
	s_setprio 1
	s_waitcnt lgkmcnt(0)
	v_mfma_scale_f32_16x16x128_f8f6f4 v[134:137], v[210:217], v[178:185], v[134:137], v1, v1 op_sel_hi:[0,0,0]
	v_mfma_scale_f32_16x16x128_f8f6f4 v[130:133], v[218:225], v[178:185], v[130:133], v1, v1 op_sel_hi:[0,0,0]
	v_mfma_scale_f32_16x16x128_f8f6f4 v[118:121], v[210:217], v[186:193], v[118:121], v1, v1 op_sel_hi:[0,0,0]
	v_mfma_scale_f32_16x16x128_f8f6f4 v[114:117], v[218:225], v[186:193], v[114:117], v1, v1 op_sel_hi:[0,0,0]
	v_mfma_scale_f32_16x16x128_f8f6f4 v[102:105], v[210:217], v[194:201], v[102:105], v1, v1 op_sel_hi:[0,0,0]
	v_mfma_scale_f32_16x16x128_f8f6f4 v[98:101], v[218:225], v[194:201], v[98:101], v1, v1 op_sel_hi:[0,0,0]
	v_mfma_scale_f32_16x16x128_f8f6f4 v[86:89], v[210:217], v[202:209], v[86:89], v1, v1 op_sel_hi:[0,0,0]
	v_mfma_scale_f32_16x16x128_f8f6f4 v[82:85], v[218:225], v[202:209], v[82:85], v1, v1 op_sel_hi:[0,0,0]
	s_setprio 0
	s_mov_b32 m0, s49
	v_lshl_add_u64 v[164:165], v[168:169], 0, s[16:17]
	s_barrier
	ds_read_b128 v[178:181], v177 offset:49152
	ds_read_b128 v[182:185], v177 offset:50176
	ds_read_b128 v[186:189], v177 offset:51200
	ds_read_b128 v[190:193], v177 offset:52224
	ds_read_b128 v[194:197], v177 offset:53248
	ds_read_b128 v[198:201], v177 offset:54272
	ds_read_b128 v[202:205], v177 offset:55296
	ds_read_b128 v[206:209], v177 offset:56320
	global_load_lds_dwordx4 v[164:165], off
	v_lshl_add_u64 v[164:165], v[170:171], 0, s[16:17]
	s_mov_b32 m0, s50
	s_nop 0
	global_load_lds_dwordx4 v[164:165], off
	s_barrier
	s_waitcnt lgkmcnt(0)
	s_setprio 1
	s_waitcnt lgkmcnt(0)
	v_mfma_scale_f32_16x16x128_f8f6f4 v[78:81], v[2:9], v[178:185], v[78:81], v1, v1 op_sel_hi:[0,0,0]
	v_mfma_scale_f32_16x16x128_f8f6f4 v[74:77], v[10:17], v[178:185], v[74:77], v1, v1 op_sel_hi:[0,0,0]
	v_mfma_scale_f32_16x16x128_f8f6f4 v[62:65], v[2:9], v[186:193], v[62:65], v1, v1 op_sel_hi:[0,0,0]
	v_mfma_scale_f32_16x16x128_f8f6f4 v[58:61], v[10:17], v[186:193], v[58:61], v1, v1 op_sel_hi:[0,0,0]
	v_mfma_scale_f32_16x16x128_f8f6f4 v[42:45], v[2:9], v[194:201], v[42:45], v1, v1 op_sel_hi:[0,0,0]
	v_mfma_scale_f32_16x16x128_f8f6f4 v[34:37], v[10:17], v[194:201], v[34:37], v1, v1 op_sel_hi:[0,0,0]
	v_mfma_scale_f32_16x16x128_f8f6f4 v[22:25], v[2:9], v[202:209], v[22:25], v1, v1 op_sel_hi:[0,0,0]
	v_mfma_scale_f32_16x16x128_f8f6f4 v[18:21], v[10:17], v[202:209], v[18:21], v1, v1 op_sel_hi:[0,0,0]
	s_setprio 0
	s_barrier
	s_add_u32 s24, s24, 0x60080
	s_addc_u32 s25, s25, 0
	s_add_i32 s26, s27, s42
	v_lshl_add_u64 v[2:3], s[24:25], 0, v[146:147]
	s_mov_b32 m0, s26
	s_nop 0
	global_load_lds_dwordx4 v[2:3], off
	v_lshl_add_u64 v[2:3], s[24:25], 0, v[148:149]
	s_add_i32 m0, s26, 0x2000
	s_nop 0
	global_load_lds_dwordx4 v[2:3], off
	s_waitcnt vmcnt(6)
	s_barrier
	s_setprio 1
	v_mfma_scale_f32_16x16x128_f8f6f4 v[70:73], v[210:217], v[178:185], v[70:73], v1, v1 op_sel_hi:[0,0,0]
	v_mfma_scale_f32_16x16x128_f8f6f4 v[66:69], v[218:225], v[178:185], v[66:69], v1, v1 op_sel_hi:[0,0,0]
	v_mfma_scale_f32_16x16x128_f8f6f4 v[46:49], v[210:217], v[186:193], v[46:49], v1, v1 op_sel_hi:[0,0,0]
	v_mfma_scale_f32_16x16x128_f8f6f4 v[38:41], v[218:225], v[186:193], v[38:41], v1, v1 op_sel_hi:[0,0,0]
	v_mfma_scale_f32_16x16x128_f8f6f4 v[50:53], v[210:217], v[194:201], v[50:53], v1, v1 op_sel_hi:[0,0,0]
	v_mfma_scale_f32_16x16x128_f8f6f4 v[54:57], v[218:225], v[194:201], v[54:57], v1, v1 op_sel_hi:[0,0,0]
	v_mfma_scale_f32_16x16x128_f8f6f4 v[26:29], v[210:217], v[202:209], v[26:29], v1, v1 op_sel_hi:[0,0,0]
	v_mfma_scale_f32_16x16x128_f8f6f4 v[30:33], v[218:225], v[202:209], v[30:33], v1, v1 op_sel_hi:[0,0,0]
	s_setprio 0
	s_add_i32 s58, s58, 2
	s_add_u32 s56, s56, 0x100
	s_addc_u32 s57, s57, 0
	s_cmp_gt_u32 s58, 13
	s_mov_b64 s[26:27], s[22:23]
	s_barrier
	s_cbranch_scc0 .LBB0_2143
	v_lshl_add_u32 v2, s55, 8, v174
	s_lshl_b32 s22, s54, 8
	s_ashr_i32 s23, s22, 31
	v_ashrrev_i32_e32 v3, 31, v2
	v_lshl_add_u64 v[4:5], v[158:159], 0, s[22:23]
	v_lshlrev_b64 v[6:7], 11, v[2:3]
	v_lshl_add_u64 v[6:7], v[4:5], 0, v[6:7]
	s_nop 15
	s_nop 15
	global_load_dwordx4 v[10:13], v[6:7], off
	v_or_b32_e32 v164, 16, v2
	v_ashrrev_i32_e32 v165, 31, v164
	v_lshlrev_b64 v[6:7], 11, v[164:165]
	v_lshl_add_u64 v[6:7], v[4:5], 0, v[6:7]
	global_load_dwordx4 v[14:17], v[6:7], off
	v_or_b32_e32 v178, 32, v2
	v_or_b32_e32 v8, 48, v2
	v_or_b32_e32 v6, s22, v176
	v_ashrrev_i32_e32 v179, 31, v178
	v_ashrrev_i32_e32 v9, 31, v8
	v_ashrrev_i32_e32 v7, 31, v6
	v_lshlrev_b64 v[166:167], 12, v[2:3]
	v_lshlrev_b64 v[168:169], 11, v[178:179]
	v_lshlrev_b64 v[170:171], 11, v[8:9]
	v_lshl_add_u64 v[166:167], s[66:67], 0, v[166:167]
	v_lshlrev_b64 v[6:7], 1, v[6:7]
	v_lshlrev_b64 v[180:181], 12, v[164:165]
	v_lshl_add_u64 v[164:165], v[4:5], 0, v[168:169]
	v_lshl_add_u64 v[168:169], v[4:5], 0, v[170:171]
	v_lshl_add_u64 v[182:183], v[166:167], 0, v[6:7]
	global_load_dwordx4 v[164:167], v[164:165], off
	s_nop 0
	global_load_dwordx4 v[168:171], v[168:169], off
	v_add_u32_e32 v214, 0x80, v2
	v_ashrrev_i32_e32 v215, 31, v214
	v_lshlrev_b64 v[214:215], 11, v[214:215]
	v_lshl_add_u64 v[214:215], v[4:5], 0, v[214:215]
	global_load_dwordx4 v[198:201], v[214:215], off
	v_add_u32_e32 v214, 0x90, v2
	v_ashrrev_i32_e32 v215, 31, v214
	v_lshlrev_b64 v[214:215], 11, v[214:215]
	v_lshl_add_u64 v[214:215], v[4:5], 0, v[214:215]
	global_load_dwordx4 v[202:205], v[214:215], off
	v_add_u32_e32 v214, 0xa0, v2
	v_ashrrev_i32_e32 v215, 31, v214
	v_lshlrev_b64 v[214:215], 11, v[214:215]
	v_lshl_add_u64 v[214:215], v[4:5], 0, v[214:215]
	global_load_dwordx4 v[206:209], v[214:215], off
	v_add_u32_e32 v214, 0xb0, v2
	v_ashrrev_i32_e32 v215, 31, v214
	v_lshlrev_b64 v[214:215], 11, v[214:215]
	v_lshl_add_u64 v[214:215], v[4:5], 0, v[214:215]
	global_load_dwordx4 v[210:213], v[214:215], off
	v_lshlrev_b64 v[8:9], 12, v[8:9]
	v_lshl_add_u64 v[8:9], s[66:67], 0, v[8:9]
	s_and_b64 vcc, exec, s[18:19]
	s_mov_b32 s54, s52
	s_mov_b32 s55, s53
	s_mov_b64 s[22:23], s[8:9]
	s_mov_b64 s[26:27], s[20:21]
	s_waitcnt vmcnt(4)
	v_cvt_f32_ubyte0_e32 v3, v10
	v_cvt_f32_ubyte1_e32 v184, v10
	v_cvt_f32_ubyte2_e32 v185, v10
	v_cvt_f32_ubyte3_e32 v10, v10
	v_cvt_f32_ubyte0_e32 v186, v11
	v_cvt_f32_ubyte1_e32 v187, v11
	v_cvt_f32_ubyte2_e32 v188, v11
	v_cvt_f32_ubyte3_e32 v11, v11
	v_cvt_f32_ubyte0_e32 v189, v12
	v_cvt_f32_ubyte1_e32 v190, v12
	v_cvt_f32_ubyte2_e32 v191, v12
	v_cvt_f32_ubyte3_e32 v12, v12
	v_cvt_f32_ubyte0_e32 v192, v13
	v_cvt_f32_ubyte1_e32 v193, v13
	v_cvt_f32_ubyte2_e32 v194, v13
	v_cvt_f32_ubyte3_e32 v13, v13
	v_mul_f32_e32 v3, v142, v3
	v_mul_f32_e32 v142, v143, v184
	v_mul_f32_e32 v10, v145, v10
	v_mul_f32_e32 v138, v138, v186
	v_mul_f32_e32 v139, v139, v187
	v_mul_f32_e32 v143, v144, v185
	v_mul_f32_e32 v140, v140, v188
	v_mul_f32_e32 v11, v141, v11
	v_mul_f32_e32 v134, v134, v189
	v_mul_f32_e32 v135, v135, v190
	v_mul_f32_e32 v12, v137, v12
	v_mul_f32_e32 v13, v133, v13
	v_mul_f32_e32 v3, 0x37008081, v3
	v_mul_f32_e32 v137, 0x37008081, v142
	v_mul_f32_e32 v141, 0x37008081, v10
	v_cvt_pk_bf16_f32 v10, v3, v137
	v_mul_f32_e32 v130, v130, v192
	v_mul_f32_e32 v131, v131, v193
	v_mul_f32_e32 v136, v136, v191
	v_mul_f32_e32 v132, v132, v194
	v_mul_f32_e32 v133, 0x37008081, v138
	v_mul_f32_e32 v138, 0x37008081, v139
	v_mul_f32_e32 v139, 0x37008081, v143
	v_mul_f32_e32 v140, 0x37008081, v140
	v_mul_f32_e32 v142, 0x37008081, v11
	v_mul_f32_e32 v134, 0x37008081, v134
	v_mul_f32_e32 v135, 0x37008081, v135
	v_mul_f32_e32 v143, 0x37008081, v12
	v_mul_f32_e32 v144, 0x37008081, v13
	v_cvt_pk_bf16_f32 v11, v139, v141
	v_cvt_pk_bf16_f32 v12, v133, v138
	v_cvt_pk_bf16_f32 v13, v140, v142
	global_store_dwordx4 v[182:183], v[10:13], off
	v_mul_f32_e32 v130, 0x37008081, v130
	v_mul_f32_e32 v131, 0x37008081, v131
	v_cvt_pk_bf16_f32 v10, v134, v135
	v_mul_f32_e32 v136, 0x37008081, v136
	v_mul_f32_e32 v132, 0x37008081, v132
	v_cvt_pk_bf16_f32 v11, v136, v143
	v_cvt_pk_bf16_f32 v12, v130, v131
	v_cvt_pk_bf16_f32 v13, v132, v144
	global_store_dwordx4 v[182:183], v[10:13], off offset:256
	v_cvt_f32_ubyte0_e32 v3, v14
	v_cvt_f32_ubyte2_e32 v130, v15
	v_cvt_f32_ubyte1_e32 v10, v14
	v_cvt_f32_ubyte2_e32 v11, v14
	v_cvt_f32_ubyte3_e32 v12, v14
	v_cvt_f32_ubyte0_e32 v13, v15
	v_cvt_f32_ubyte1_e32 v14, v15
	v_mul_f32_e32 v10, v127, v10
	v_mul_f32_e32 v13, v122, v13
	v_mul_f32_e32 v122, 0x37008081, v10
	v_mul_f32_e32 v10, v123, v14
	v_mul_f32_e32 v123, 0x37008081, v10
	v_mul_f32_e32 v10, v128, v11
	v_mul_f32_e32 v3, v126, v3
	v_mul_f32_e32 v126, 0x37008081, v10
	v_mul_f32_e32 v10, v124, v130
	v_cvt_f32_ubyte3_e32 v15, v15
	v_mul_f32_e32 v124, 0x37008081, v10
	v_mul_f32_e32 v10, v129, v12
	v_mul_f32_e32 v12, 0x37008081, v10
	v_mul_f32_e32 v10, v125, v15
	v_mul_f32_e32 v13, 0x37008081, v13
	v_mul_f32_e32 v125, 0x37008081, v10
	v_lshl_add_u64 v[10:11], s[66:67], 0, v[180:181]
	v_mul_f32_e32 v3, 0x37008081, v3
	v_lshl_add_u64 v[14:15], v[10:11], 0, v[6:7]
	v_cvt_pk_bf16_f32 v10, v3, v122
	v_cvt_pk_bf16_f32 v11, v126, v12
	v_cvt_pk_bf16_f32 v12, v13, v123
	v_cvt_pk_bf16_f32 v13, v124, v125
	global_store_dwordx4 v[14:15], v[10:13], off
	v_cvt_f32_ubyte0_e32 v3, v16
	v_cvt_f32_ubyte2_e32 v122, v17
	v_cvt_f32_ubyte1_e32 v10, v16
	v_cvt_f32_ubyte2_e32 v11, v16
	v_cvt_f32_ubyte3_e32 v12, v16
	v_cvt_f32_ubyte0_e32 v13, v17
	v_cvt_f32_ubyte1_e32 v16, v17
	v_cvt_f32_ubyte3_e32 v17, v17
	v_mul_f32_e32 v13, v114, v13
	v_mul_f32_e32 v10, v119, v10
	v_mul_f32_e32 v11, v120, v11
	v_mul_f32_e32 v12, v121, v12
	v_mul_f32_e32 v3, v118, v3
	v_mul_f32_e32 v13, 0x37008081, v13
	v_mul_f32_e32 v10, 0x37008081, v10
	v_mul_f32_e32 v16, v115, v16
	v_mul_f32_e32 v11, 0x37008081, v11
	v_mul_f32_e32 v114, v116, v122
	v_mul_f32_e32 v12, 0x37008081, v12
	v_mul_f32_e32 v17, v117, v17
	v_mul_f32_e32 v3, 0x37008081, v3
	v_mul_f32_e32 v16, 0x37008081, v16
	v_mul_f32_e32 v114, 0x37008081, v114
	v_mul_f32_e32 v17, 0x37008081, v17
	v_cvt_pk_bf16_f32 v10, v3, v10
	v_cvt_pk_bf16_f32 v11, v11, v12
	v_cvt_pk_bf16_f32 v12, v13, v16
	v_cvt_pk_bf16_f32 v13, v114, v17
	global_store_dwordx4 v[14:15], v[10:13], off offset:256
	v_cvt_f32_ubyte0_e32 v15, v165
	v_cvt_f32_ubyte3_e32 v14, v164
	v_cvt_f32_ubyte1_e32 v12, v164
	v_cvt_f32_ubyte2_e32 v13, v164
	v_cvt_f32_ubyte1_e32 v16, v165
	v_mul_f32_e32 v15, v106, v15
	v_lshlrev_b64 v[10:11], 12, v[178:179]
	v_cvt_f32_ubyte0_e32 v3, v164
	v_cvt_f32_ubyte2_e32 v17, v165
	v_cvt_f32_ubyte3_e32 v114, v165
	v_mul_f32_e32 v106, 0x37008081, v15
	v_mul_f32_e32 v12, v111, v12
	v_mul_f32_e32 v15, v107, v16
	v_mul_f32_e32 v13, v112, v13
	v_mul_f32_e32 v14, v113, v14
	v_mul_f32_e32 v3, v110, v3
	v_mul_f32_e32 v12, 0x37008081, v12
	v_mul_f32_e32 v16, 0x37008081, v15
	v_mul_f32_e32 v13, 0x37008081, v13
	v_mul_f32_e32 v15, v108, v17
	v_mul_f32_e32 v107, 0x37008081, v14
	v_mul_f32_e32 v14, v109, v114
	v_lshl_add_u64 v[10:11], s[66:67], 0, v[10:11]
	v_mul_f32_e32 v3, 0x37008081, v3
	v_mul_f32_e32 v17, 0x37008081, v15
	v_mul_f32_e32 v108, 0x37008081, v14
	v_lshl_add_u64 v[14:15], v[10:11], 0, v[6:7]
	v_cvt_pk_bf16_f32 v10, v3, v12
	v_cvt_pk_bf16_f32 v11, v13, v107
	v_cvt_pk_bf16_f32 v12, v106, v16
	v_cvt_pk_bf16_f32 v13, v17, v108
	global_store_dwordx4 v[14:15], v[10:13], off
	v_cvt_f32_ubyte0_e32 v3, v166
	v_cvt_f32_ubyte1_e32 v16, v167
	v_cvt_f32_ubyte1_e32 v10, v166
	v_cvt_f32_ubyte2_e32 v11, v166
	v_cvt_f32_ubyte3_e32 v12, v166
	v_cvt_f32_ubyte0_e32 v13, v167
	v_cvt_f32_ubyte2_e32 v17, v167
	v_cvt_f32_ubyte3_e32 v106, v167
	v_mul_f32_e32 v13, v98, v13
	v_mul_f32_e32 v10, v103, v10
	v_mul_f32_e32 v11, v104, v11
	v_mul_f32_e32 v12, v105, v12
	v_mul_f32_e32 v3, v102, v3
	v_mul_f32_e32 v13, 0x37008081, v13
	v_mul_f32_e32 v10, 0x37008081, v10
	v_mul_f32_e32 v16, v99, v16
	v_mul_f32_e32 v11, 0x37008081, v11
	v_mul_f32_e32 v17, v100, v17
	v_mul_f32_e32 v12, 0x37008081, v12
	v_mul_f32_e32 v98, v101, v106
	v_mul_f32_e32 v3, 0x37008081, v3
	v_mul_f32_e32 v16, 0x37008081, v16
	v_mul_f32_e32 v17, 0x37008081, v17
	v_mul_f32_e32 v98, 0x37008081, v98
	v_cvt_pk_bf16_f32 v10, v3, v10
	v_cvt_pk_bf16_f32 v11, v11, v12
	v_cvt_pk_bf16_f32 v12, v13, v16
	v_cvt_pk_bf16_f32 v13, v17, v98
	global_store_dwordx4 v[14:15], v[10:13], off offset:256
	v_cvt_f32_ubyte1_e32 v14, v169
	v_cvt_f32_ubyte0_e32 v3, v168
	v_cvt_f32_ubyte0_e32 v13, v169
	v_cvt_f32_ubyte1_e32 v10, v168
	v_cvt_f32_ubyte2_e32 v11, v168
	v_cvt_f32_ubyte3_e32 v12, v168
	v_mul_f32_e32 v13, v90, v13
	v_cvt_f32_ubyte2_e32 v15, v169
	v_cvt_f32_ubyte3_e32 v16, v169
	v_mul_f32_e32 v17, 0x37008081, v13
	v_mul_f32_e32 v10, v95, v10
	v_mul_f32_e32 v13, v91, v14
	v_mul_f32_e32 v11, v96, v11
	v_mul_f32_e32 v12, v97, v12
	v_mul_f32_e32 v3, v94, v3
	v_mul_f32_e32 v10, 0x37008081, v10
	v_mul_f32_e32 v14, 0x37008081, v13
	v_mul_f32_e32 v11, 0x37008081, v11
	v_mul_f32_e32 v13, v92, v15
	v_mul_f32_e32 v90, 0x37008081, v12
	v_mul_f32_e32 v12, v93, v16
	v_mul_f32_e32 v3, 0x37008081, v3
	v_mul_f32_e32 v15, 0x37008081, v13
	v_mul_f32_e32 v16, 0x37008081, v12
	v_lshl_add_u64 v[12:13], v[8:9], 0, v[6:7]
	v_cvt_pk_bf16_f32 v8, v3, v10
	v_cvt_pk_bf16_f32 v9, v11, v90
	v_cvt_pk_bf16_f32 v10, v17, v14
	v_cvt_pk_bf16_f32 v11, v15, v16
	global_store_dwordx4 v[12:13], v[8:11], off
	v_cvt_f32_ubyte3_e32 v16, v171
	v_cvt_f32_ubyte0_e32 v3, v170
	v_cvt_f32_ubyte1_e32 v8, v170
	v_cvt_f32_ubyte2_e32 v9, v170
	v_cvt_f32_ubyte3_e32 v10, v170
	v_cvt_f32_ubyte0_e32 v11, v171
	v_cvt_f32_ubyte1_e32 v14, v171
	v_cvt_f32_ubyte2_e32 v15, v171
	v_mul_f32_e32 v11, v82, v11
	v_mul_f32_e32 v8, v87, v8
	v_mul_f32_e32 v9, v88, v9
	v_mul_f32_e32 v10, v89, v10
	v_mul_f32_e32 v16, v85, v16
	v_mul_f32_e32 v3, v86, v3
	v_mul_f32_e32 v11, 0x37008081, v11
	v_mul_f32_e32 v8, 0x37008081, v8
	v_mul_f32_e32 v14, v83, v14
	v_mul_f32_e32 v9, 0x37008081, v9
	v_mul_f32_e32 v15, v84, v15
	v_mul_f32_e32 v10, 0x37008081, v10
	v_mul_f32_e32 v16, 0x37008081, v16
	v_mul_f32_e32 v3, 0x37008081, v3
	v_mul_f32_e32 v14, 0x37008081, v14
	v_mul_f32_e32 v15, 0x37008081, v15
	v_cvt_pk_bf16_f32 v8, v3, v8
	v_cvt_pk_bf16_f32 v9, v9, v10
	v_cvt_pk_bf16_f32 v10, v11, v14
	v_cvt_pk_bf16_f32 v11, v15, v16
	v_add_u32_e32 v16, 0x80, v2
	v_ashrrev_i32_e32 v17, 31, v16
	global_store_dwordx4 v[12:13], v[8:11], off offset:256
	v_add_u32_e32 v86, 0x90, v2
	v_ashrrev_i32_e32 v87, 31, v86
	v_add_u32_e32 v88, 0xa0, v2
	v_add_u32_e32 v90, 0xb0, v2
	v_ashrrev_i32_e32 v89, 31, v88
	v_ashrrev_i32_e32 v91, 31, v90
	v_lshlrev_b64 v[16:17], 12, v[16:17]
	s_waitcnt vmcnt(8)
	v_mov_b32_e32 v12, v202
	v_mov_b32_e32 v13, v203
	v_mov_b32_e32 v14, v204
	v_mov_b32_e32 v15, v205
	v_mov_b32_e32 v82, v206
	v_mov_b32_e32 v83, v207
	v_mov_b32_e32 v84, v208
	v_mov_b32_e32 v85, v209
	v_mov_b32_e32 v8, v198
	v_mov_b32_e32 v9, v199
	v_mov_b32_e32 v10, v200
	v_mov_b32_e32 v11, v201
	v_mov_b32_e32 v2, v210
	v_mov_b32_e32 v3, v211
	v_mov_b32_e32 v4, v212
	v_mov_b32_e32 v5, v213
	s_nop 0
	s_nop 0
	s_nop 0
	s_nop 0
	s_nop 0
	v_cvt_f32_ubyte0_e32 v92, v8
	v_cvt_f32_ubyte1_e32 v93, v8
	v_cvt_f32_ubyte2_e32 v94, v8
	v_cvt_f32_ubyte3_e32 v8, v8
	v_cvt_f32_ubyte0_e32 v95, v9
	v_cvt_f32_ubyte1_e32 v96, v9
	v_cvt_f32_ubyte2_e32 v97, v9
	v_cvt_f32_ubyte3_e32 v9, v9
	v_mul_f32_e32 v74, v74, v95
	v_mul_f32_e32 v75, v75, v96
	v_mul_f32_e32 v76, v76, v97
	v_mul_f32_e32 v8, v81, v8
	v_mul_f32_e32 v78, v78, v92
	v_mul_f32_e32 v92, 0x37008081, v74
	v_mul_f32_e32 v74, v79, v93
	v_mul_f32_e32 v79, 0x37008081, v75
	v_mul_f32_e32 v75, v80, v94
	v_mul_f32_e32 v80, 0x37008081, v76
	v_mul_f32_e32 v76, 0x37008081, v8
	v_mul_f32_e32 v8, v77, v9
	v_mul_f32_e32 v74, 0x37008081, v74
	v_mul_f32_e32 v75, 0x37008081, v75
	v_mul_f32_e32 v77, 0x37008081, v8
	v_lshl_add_u64 v[8:9], s[66:67], 0, v[16:17]
	v_mul_f32_e32 v78, 0x37008081, v78
	v_lshl_add_u64 v[16:17], v[8:9], 0, v[6:7]
	v_cvt_pk_bf16_f32 v74, v78, v74
	v_cvt_pk_bf16_f32 v75, v75, v76
	v_cvt_pk_bf16_f32 v76, v92, v79
	v_cvt_pk_bf16_f32 v77, v80, v77
	global_store_dwordx4 v[16:17], v[74:77], off
	v_cvt_f32_ubyte0_e32 v8, v10
	v_cvt_f32_ubyte1_e32 v9, v10
	v_cvt_f32_ubyte2_e32 v74, v10
	v_cvt_f32_ubyte3_e32 v10, v10
	v_cvt_f32_ubyte0_e32 v75, v11
	v_cvt_f32_ubyte1_e32 v76, v11
	v_cvt_f32_ubyte2_e32 v77, v11
	v_cvt_f32_ubyte3_e32 v11, v11
	v_mul_f32_e32 v8, v70, v8
	v_mul_f32_e32 v9, v71, v9
	v_mul_f32_e32 v10, v73, v10
	v_mul_f32_e32 v11, v69, v11
	v_mul_f32_e32 v8, 0x37008081, v8
	v_mul_f32_e32 v66, v66, v75
	v_mul_f32_e32 v9, 0x37008081, v9
	v_mul_f32_e32 v67, v67, v76
	v_mul_f32_e32 v70, v72, v74
	v_mul_f32_e32 v68, v68, v77
	v_mul_f32_e32 v10, 0x37008081, v10
	v_mul_f32_e32 v11, 0x37008081, v11
	v_mul_f32_e32 v66, 0x37008081, v66
	v_mul_f32_e32 v67, 0x37008081, v67
	v_mul_f32_e32 v70, 0x37008081, v70
	v_mul_f32_e32 v68, 0x37008081, v68
	v_cvt_pk_bf16_f32 v8, v8, v9
	v_cvt_pk_bf16_f32 v9, v70, v10
	v_cvt_pk_bf16_f32 v10, v66, v67
	v_cvt_pk_bf16_f32 v11, v68, v11
	global_store_dwordx4 v[16:17], v[8:11], off offset:256
	v_cvt_f32_ubyte2_e32 v16, v12
	v_cvt_f32_ubyte0_e32 v17, v13
	v_cvt_f32_ubyte0_e32 v10, v12
	v_cvt_f32_ubyte1_e32 v11, v12
	v_cvt_f32_ubyte3_e32 v12, v12
	v_lshlrev_b64 v[8:9], 12, v[86:87]
	v_cvt_f32_ubyte1_e32 v66, v13
	v_cvt_f32_ubyte2_e32 v67, v13
	v_cvt_f32_ubyte3_e32 v13, v13
	v_mul_f32_e32 v10, v62, v10
	v_mul_f32_e32 v11, v63, v11
	v_mul_f32_e32 v12, v65, v12
	v_mul_f32_e32 v10, 0x37008081, v10
	v_mul_f32_e32 v17, v58, v17
	v_mul_f32_e32 v11, 0x37008081, v11
	v_mul_f32_e32 v58, v59, v66
	v_mul_f32_e32 v16, v64, v16
	v_mul_f32_e32 v59, v60, v67
	v_mul_f32_e32 v60, 0x37008081, v12
	v_mul_f32_e32 v12, v61, v13
	v_lshl_add_u64 v[8:9], s[66:67], 0, v[8:9]
	v_mul_f32_e32 v17, 0x37008081, v17
	v_mul_f32_e32 v58, 0x37008081, v58
	v_mul_f32_e32 v16, 0x37008081, v16
	v_mul_f32_e32 v59, 0x37008081, v59
	v_mul_f32_e32 v61, 0x37008081, v12
	v_lshl_add_u64 v[12:13], v[8:9], 0, v[6:7]
	v_cvt_pk_bf16_f32 v8, v10, v11
	v_cvt_pk_bf16_f32 v9, v16, v60
	v_cvt_pk_bf16_f32 v10, v17, v58
	v_cvt_pk_bf16_f32 v11, v59, v61
	global_store_dwordx4 v[12:13], v[8:11], off
	v_cvt_f32_ubyte1_e32 v16, v15
	v_cvt_f32_ubyte2_e32 v17, v15
	v_cvt_f32_ubyte0_e32 v8, v14
	v_cvt_f32_ubyte1_e32 v9, v14
	v_cvt_f32_ubyte2_e32 v10, v14
	v_cvt_f32_ubyte3_e32 v11, v14
	v_cvt_f32_ubyte0_e32 v14, v15
	v_cvt_f32_ubyte3_e32 v15, v15
	v_mul_f32_e32 v8, v46, v8
	v_mul_f32_e32 v9, v47, v9
	v_mul_f32_e32 v10, v48, v10
	v_mul_f32_e32 v11, v49, v11
	v_mul_f32_e32 v8, 0x37008081, v8
	v_mul_f32_e32 v14, v38, v14
	v_mul_f32_e32 v9, 0x37008081, v9
	v_mul_f32_e32 v16, v39, v16
	v_mul_f32_e32 v10, 0x37008081, v10
	v_mul_f32_e32 v17, v40, v17
	v_mul_f32_e32 v11, 0x37008081, v11
	v_mul_f32_e32 v15, v41, v15
	v_mul_f32_e32 v14, 0x37008081, v14
	v_mul_f32_e32 v16, 0x37008081, v16
	v_mul_f32_e32 v17, 0x37008081, v17
	v_mul_f32_e32 v15, 0x37008081, v15
	v_cvt_pk_bf16_f32 v8, v8, v9
	v_cvt_pk_bf16_f32 v9, v10, v11
	v_cvt_pk_bf16_f32 v10, v14, v16
	v_cvt_pk_bf16_f32 v11, v17, v15
	global_store_dwordx4 v[12:13], v[8:11], off offset:256
	v_cvt_f32_ubyte2_e32 v12, v82
	v_cvt_f32_ubyte0_e32 v14, v83
	v_cvt_f32_ubyte2_e32 v16, v83
	v_mul_f32_e32 v12, v44, v12
	v_cvt_f32_ubyte0_e32 v10, v82
	v_cvt_f32_ubyte3_e32 v13, v82
	v_mul_f32_e32 v14, v34, v14
	v_mul_f32_e32 v34, 0x37008081, v12
	v_mul_f32_e32 v12, v36, v16
	v_lshlrev_b64 v[8:9], 12, v[88:89]
	v_cvt_f32_ubyte1_e32 v11, v82
	v_cvt_f32_ubyte1_e32 v15, v83
	v_cvt_f32_ubyte3_e32 v17, v83
	v_mul_f32_e32 v10, v42, v10
	v_mul_f32_e32 v16, 0x37008081, v12
	v_mul_f32_e32 v12, v45, v13
	v_mul_f32_e32 v10, 0x37008081, v10
	v_mul_f32_e32 v11, v43, v11
	v_mul_f32_e32 v15, v35, v15
	v_mul_f32_e32 v35, 0x37008081, v12
	v_mul_f32_e32 v12, v37, v17
	v_lshl_add_u64 v[8:9], s[66:67], 0, v[8:9]
	v_mul_f32_e32 v14, 0x37008081, v14
	v_mul_f32_e32 v11, 0x37008081, v11
	v_mul_f32_e32 v15, 0x37008081, v15
	v_mul_f32_e32 v17, 0x37008081, v12
	v_lshl_add_u64 v[12:13], v[8:9], 0, v[6:7]
	v_cvt_pk_bf16_f32 v8, v10, v11
	v_cvt_pk_bf16_f32 v9, v34, v35
	v_cvt_pk_bf16_f32 v10, v14, v15
	v_cvt_pk_bf16_f32 v11, v16, v17
	global_store_dwordx4 v[12:13], v[8:11], off
	v_cvt_f32_ubyte0_e32 v14, v85
	v_cvt_f32_ubyte1_e32 v15, v85
	v_cvt_f32_ubyte0_e32 v8, v84
	v_cvt_f32_ubyte1_e32 v9, v84
	v_cvt_f32_ubyte2_e32 v10, v84
	v_cvt_f32_ubyte3_e32 v11, v84
	v_mul_f32_e32 v8, v50, v8
	v_mul_f32_e32 v9, v51, v9
	v_mul_f32_e32 v10, v52, v10
	v_cvt_f32_ubyte2_e32 v16, v85
	v_cvt_f32_ubyte3_e32 v17, v85
	v_mul_f32_e32 v8, 0x37008081, v8
	v_mul_f32_e32 v14, v54, v14
	v_mul_f32_e32 v9, 0x37008081, v9
	v_mul_f32_e32 v15, v55, v15
	v_mul_f32_e32 v10, 0x37008081, v10
	v_mul_f32_e32 v11, v53, v11
	v_mul_f32_e32 v14, 0x37008081, v14
	v_mul_f32_e32 v15, 0x37008081, v15
	v_mul_f32_e32 v16, v56, v16
	v_mul_f32_e32 v11, 0x37008081, v11
	v_mul_f32_e32 v17, v57, v17
	v_cvt_pk_bf16_f32 v8, v8, v9
	v_cvt_pk_bf16_f32 v9, v10, v11
	v_cvt_pk_bf16_f32 v10, v14, v15
	v_mul_f32_e32 v16, 0x37008081, v16
	v_mul_f32_e32 v17, 0x37008081, v17
	v_cvt_pk_bf16_f32 v11, v16, v17
	global_store_dwordx4 v[12:13], v[8:11], off offset:256
	v_cvt_f32_ubyte0_e32 v13, v3
	v_cvt_f32_ubyte2_e32 v12, v2
	v_cvt_f32_ubyte0_e32 v10, v2
	v_mul_f32_e32 v10, v22, v10
	v_cvt_f32_ubyte1_e32 v11, v2
	v_mul_f32_e32 v16, 0x37008081, v10
	v_mul_f32_e32 v10, v18, v13
	v_cvt_f32_ubyte3_e32 v2, v2
	v_cvt_f32_ubyte1_e32 v14, v3
	v_mul_f32_e32 v13, 0x37008081, v10
	v_mul_f32_e32 v10, v23, v11
	v_cvt_f32_ubyte2_e32 v15, v3
	v_cvt_f32_ubyte3_e32 v3, v3
	v_mul_f32_e32 v17, 0x37008081, v10
	v_mul_f32_e32 v10, v19, v14
	v_mul_f32_e32 v2, v25, v2
	v_lshlrev_b64 v[8:9], 12, v[90:91]
	v_mul_f32_e32 v14, 0x37008081, v10
	v_mul_f32_e32 v10, v24, v12
	v_mul_f32_e32 v18, 0x37008081, v2
	v_mul_f32_e32 v2, v21, v3
	v_mul_f32_e32 v12, 0x37008081, v10
	v_mul_f32_e32 v10, v20, v15
	v_mul_f32_e32 v19, 0x37008081, v2
	v_lshl_add_u64 v[2:3], s[66:67], 0, v[8:9]
	v_mul_f32_e32 v15, 0x37008081, v10
	v_lshl_add_u64 v[10:11], v[2:3], 0, v[6:7]
	v_cvt_pk_bf16_f32 v6, v16, v17
	v_cvt_pk_bf16_f32 v7, v12, v18
	v_cvt_pk_bf16_f32 v8, v13, v14
	v_cvt_pk_bf16_f32 v9, v15, v19
	global_store_dwordx4 v[10:11], v[6:9], off
	v_cvt_f32_ubyte0_e32 v2, v4
	v_cvt_f32_ubyte1_e32 v3, v4
	v_cvt_f32_ubyte2_e32 v6, v4
	v_cvt_f32_ubyte3_e32 v4, v4
	v_cvt_f32_ubyte0_e32 v7, v5
	v_cvt_f32_ubyte1_e32 v8, v5
	v_cvt_f32_ubyte2_e32 v9, v5
	v_cvt_f32_ubyte3_e32 v5, v5
	v_mul_f32_e32 v2, v26, v2
	v_mul_f32_e32 v3, v27, v3
	v_mul_f32_e32 v4, v29, v4
	v_mul_f32_e32 v5, v33, v5
	v_mul_f32_e32 v2, 0x37008081, v2
	v_mul_f32_e32 v7, v30, v7
	v_mul_f32_e32 v3, 0x37008081, v3
	v_mul_f32_e32 v8, v31, v8
	v_mul_f32_e32 v6, v28, v6
	v_mul_f32_e32 v9, v32, v9
	v_mul_f32_e32 v4, 0x37008081, v4
	v_mul_f32_e32 v5, 0x37008081, v5
	v_mul_f32_e32 v7, 0x37008081, v7
	v_mul_f32_e32 v8, 0x37008081, v8
	v_mul_f32_e32 v6, 0x37008081, v6
	v_mul_f32_e32 v9, 0x37008081, v9
	v_cvt_pk_bf16_f32 v2, v2, v3
	v_cvt_pk_bf16_f32 v3, v6, v4
	v_cvt_pk_bf16_f32 v4, v7, v8
	v_cvt_pk_bf16_f32 v5, v9, v5
	global_store_dwordx4 v[10:11], v[2:5], off offset:256
	s_cbranch_vccz .LBB0_2136
	s_waitcnt vmcnt(0)
	s_cmpk_gt_u32 s41, 0xff
	s_cbranch_scc1 .LBB0_2130
	s_barrier
	s_branch .LBB0_2130
